# stack7 with the L2 touches limited to units whose operand is HBM-resident (P6 units >= 7, P1 units >= 3, none in P3)
# speedup vs baseline: 1.0034x; 1.0034x over previous
; template <class Epi, class Sched>
; __device__ __forceinline__ void gemm_phase(LAS unsigned char* lds, const Sched& S, const Epi& E, const int wid) {
;     ...
;         for (int t = 0; t < nt; t += 2) {
;             const bool last = (t == nt - 2);
;             const char* a1 = cA + (size_t)(t + 1) * kstep;
;             const char* a2 = last ? nA : cA + (size_t)(t + 2) * kstep; const char* b2 = last ? nB : cB + (size_t)(t + 2) * kstep;
;             const char* a3 = a2 + kstep; const char* b3 = b2 + kstep;
.LBB7_219:
	s_cmp_gt_u32 s94, 1
	s_cbranch_scc1 .Lp1_notouch
	s_cmp_lt_u32 s73, 4
	s_cbranch_scc1 .Lp1_notouch
	s_sub_i32 s100, s75, 10
	s_lshl_b32 s100, s100, 7
	s_cmp_gt_i32 s75, 8
	s_cselect_b32 s98, s36, s44
	s_cselect_b32 s99, s5, s45
	s_cselect_b32 s100, s100, 0x200
	s_add_u32 s98, s98, s100
	s_addc_u32 s99, s99, 0
	s_lshl_b32 s100, s94, 7
	s_add_u32 s98, s98, s100
	s_addc_u32 s99, s99, 0
	s_lshr_b32 s100, s92, 6
	s_and_b32 s100, s100, 3
	s_lshl_b32 s100, s100, 6
	v_mbcnt_lo_u32_b32 v210, -1, 0
	v_mbcnt_hi_u32_b32 v210, -1, v210
	v_add_u32_e32 v210, s100, v210
	v_lshlrev_b32_e32 v210, 11, v210
	global_load_dword v211, v210, s[98:99]

; template <class Epi, class Sched>
; __device__ __forceinline__ void gemm_phase(LAS unsigned char* lds, const Sched& S, const Epi& E, const int wid) {
;     ...
;         for (int t = 0; t < nt; t += 2) {
;             const bool last = (t == nt - 2);
;             const char* a1 = cA + (size_t)(t + 1) * kstep;
;             const char* a2 = last ? nA : cA + (size_t)(t + 2) * kstep; const char* b2 = last ? nB : cB + (size_t)(t + 2) * kstep;
;             const char* a3 = a2 + kstep; const char* b3 = b2 + kstep;
.LBB7_869:
	s_cmp_gt_u32 s94, 1
	s_cbranch_scc1 .Lp6_notouch
	s_cmp_lt_u32 s39, 7
	s_cbranch_scc1 .Lp6_notouch
	s_sub_i32 s100, s81, 2
	s_lshl_b32 s100, s100, 7
	s_cmp_gt_i32 s81, 0
	s_cselect_b32 s98, s41, s42
	s_cselect_b32 s99, s21, s43
	s_cselect_b32 s100, s100, 0x200
	s_add_u32 s98, s98, s100
	s_addc_u32 s99, s99, 0
	s_lshl_b32 s100, s94, 7
	s_add_u32 s98, s98, s100
	s_addc_u32 s99, s99, 0
	s_and_b32 s100, s95, 3
	s_lshl_b32 s100, s100, 6
	v_mbcnt_lo_u32_b32 v255, -1, 0
	v_mbcnt_hi_u32_b32 v255, -1, v255
	v_add_u32_e32 v255, s100, v255
	v_lshlrev_b32_e32 v255, 10, v255
	global_load_dword v255, v255, s[98:99]
